# sc1 write-through stores also on the P11 expert-gather rows (on top of P1 and P10)
# baseline (speedup 1.0000x reference)
.LBB0_2244:
	v_add_co_u32_e32 v36, vcc, 0x1000, v34
	v_mov_b32_e32 v89, s13
	s_nop 0
	v_addc_co_u32_e32 v37, vcc, 0, v35, vcc
	v_add_co_u32_e32 v150, vcc, 0x2000, v34
	global_load_dwordx4 v[12:15], v[34:35], off
	global_load_dwordx4 v[16:19], v[34:35], off offset:1024
	global_load_dwordx4 v[4:7], v[34:35], off offset:2048
	global_load_dwordx4 v[8:11], v[34:35], off offset:3072
	v_addc_co_u32_e32 v151, vcc, 0, v35, vcc
	ds_read_b128 v[90:93], v89
	ds_read_b128 v[94:97], v89 offset:16
	ds_read_b128 v[98:101], v89 offset:32
	ds_read_b128 v[102:105], v89 offset:48
	ds_read_b128 v[106:109], v89 offset:64
	ds_read_b128 v[110:113], v89 offset:80
	ds_read_b128 v[114:117], v89 offset:96
	ds_read_b128 v[118:121], v89 offset:112
	global_load_dwordx4 v[122:125], v[36:37], off
	global_load_dwordx4 v[126:129], v[36:37], off offset:1024
	global_load_dwordx4 v[130:133], v[36:37], off offset:2048
	global_load_dwordx4 v[134:137], v[36:37], off offset:3072
	v_add_co_u32_e32 v36, vcc, 0x3000, v34
	global_load_dwordx4 v[138:141], v[150:151], off
	global_load_dwordx4 v[142:145], v[150:151], off offset:1024
	global_load_dwordx4 v[146:149], v[150:151], off offset:2048
	s_nop 0
	global_load_dwordx4 v[150:153], v[150:151], off offset:3072
	v_addc_co_u32_e32 v37, vcc, 0, v35, vcc
	global_load_dwordx4 v[154:157], v[36:37], off
	global_load_dwordx4 v[158:161], v[36:37], off offset:1024
	global_load_dwordx4 v[162:165], v[36:37], off offset:2048
	global_load_dwordx4 v[166:169], v[36:37], off offset:3072
	s_waitcnt lgkmcnt(7)
	v_ashrrev_i32_e32 v37, 31, v90
	v_mov_b32_e32 v36, v90
	v_add_co_u32_e64 v3, s[10:11], 64, v3
	v_ashrrev_i32_e32 v171, 31, v91
	v_mov_b32_e32 v170, v91
	v_ashrrev_i32_e32 v91, 31, v92
	v_mov_b32_e32 v90, v92
	v_ashrrev_i32_e32 v173, 31, v93
	v_mov_b32_e32 v172, v93
	s_waitcnt lgkmcnt(6)
	v_ashrrev_i32_e32 v93, 31, v94
	v_mov_b32_e32 v92, v94
	v_ashrrev_i32_e32 v175, 31, v95
	v_mov_b32_e32 v174, v95
	v_ashrrev_i32_e32 v95, 31, v96
	v_mov_b32_e32 v94, v96
	v_ashrrev_i32_e32 v177, 31, v97
	v_mov_b32_e32 v176, v97
	s_waitcnt lgkmcnt(5)
	v_ashrrev_i32_e32 v97, 31, v98
	v_mov_b32_e32 v96, v98
	v_ashrrev_i32_e32 v179, 31, v99
	v_mov_b32_e32 v178, v99
	v_ashrrev_i32_e32 v99, 31, v100
	v_mov_b32_e32 v98, v100
	v_ashrrev_i32_e32 v181, 31, v101
	v_mov_b32_e32 v180, v101
	s_waitcnt lgkmcnt(4)
	v_ashrrev_i32_e32 v101, 31, v102
	v_mov_b32_e32 v100, v102
	v_ashrrev_i32_e32 v183, 31, v103
	v_mov_b32_e32 v182, v103
	v_ashrrev_i32_e32 v103, 31, v104
	v_mov_b32_e32 v102, v104
	v_ashrrev_i32_e32 v185, 31, v105
	v_mov_b32_e32 v184, v105
	s_waitcnt lgkmcnt(3)
	v_ashrrev_i32_e32 v105, 31, v106
	v_mov_b32_e32 v104, v106
	v_ashrrev_i32_e32 v187, 31, v107
	v_mov_b32_e32 v186, v107
	v_ashrrev_i32_e32 v107, 31, v108
	v_mov_b32_e32 v106, v108
	v_ashrrev_i32_e32 v189, 31, v109
	v_mov_b32_e32 v188, v109
	s_waitcnt lgkmcnt(2)
	v_ashrrev_i32_e32 v109, 31, v110
	v_mov_b32_e32 v108, v110
	v_ashrrev_i32_e32 v191, 31, v111
	v_mov_b32_e32 v190, v111
	v_ashrrev_i32_e32 v111, 31, v112
	v_mov_b32_e32 v110, v112
	v_ashrrev_i32_e32 v193, 31, v113
	v_mov_b32_e32 v192, v113
	s_waitcnt lgkmcnt(1)
	v_ashrrev_i32_e32 v113, 31, v114
	v_mov_b32_e32 v112, v114
	v_ashrrev_i32_e32 v195, 31, v115
	v_mov_b32_e32 v194, v115
	v_ashrrev_i32_e32 v115, 31, v116
	v_mov_b32_e32 v114, v116
	v_ashrrev_i32_e32 v197, 31, v117
	v_mov_b32_e32 v196, v117
	s_waitcnt lgkmcnt(0)
	v_ashrrev_i32_e32 v117, 31, v118
	v_mov_b32_e32 v116, v118
	v_ashrrev_i32_e32 v199, 31, v119
	v_mov_b32_e32 v198, v119
	v_ashrrev_i32_e32 v119, 31, v120
	v_mov_b32_e32 v118, v120
	v_ashrrev_i32_e32 v201, 31, v121
	v_mov_b32_e32 v200, v121
	v_lshlrev_b64 v[36:37], 11, v[36:37]
	s_addk_i32 s13, 0x400
	v_lshl_add_u64 v[34:35], v[34:35], 0, s[38:39]
	s_andn2_b64 vcc, exec, s[10:11]
	v_lshlrev_b64 v[120:121], 11, v[170:171]
	v_lshlrev_b64 v[170:171], 11, v[172:173]
	v_lshlrev_b64 v[90:91], 11, v[90:91]
	v_lshlrev_b64 v[172:173], 11, v[174:175]
	v_lshlrev_b64 v[92:93], 11, v[92:93]
	v_lshlrev_b64 v[174:175], 11, v[176:177]
	v_lshlrev_b64 v[94:95], 11, v[94:95]
	v_lshlrev_b64 v[176:177], 11, v[178:179]
	v_lshlrev_b64 v[96:97], 11, v[96:97]
	v_lshlrev_b64 v[178:179], 11, v[180:181]
	v_lshlrev_b64 v[98:99], 11, v[98:99]
	v_lshlrev_b64 v[180:181], 11, v[182:183]
	v_lshlrev_b64 v[100:101], 11, v[100:101]
	v_lshlrev_b64 v[182:183], 11, v[184:185]
	v_lshlrev_b64 v[102:103], 11, v[102:103]
	v_lshlrev_b64 v[184:185], 11, v[186:187]
	v_lshlrev_b64 v[104:105], 11, v[104:105]
	v_lshlrev_b64 v[186:187], 11, v[188:189]
	v_lshlrev_b64 v[106:107], 11, v[106:107]
	v_lshlrev_b64 v[188:189], 11, v[190:191]
	v_lshlrev_b64 v[108:109], 11, v[108:109]
	v_lshlrev_b64 v[190:191], 11, v[192:193]
	v_lshlrev_b64 v[110:111], 11, v[110:111]
	v_lshlrev_b64 v[192:193], 11, v[194:195]
	v_lshlrev_b64 v[112:113], 11, v[112:113]
	v_lshlrev_b64 v[194:195], 11, v[196:197]
	v_lshlrev_b64 v[114:115], 11, v[114:115]
	v_lshlrev_b64 v[196:197], 11, v[198:199]
	v_lshlrev_b64 v[116:117], 11, v[116:117]
	v_lshlrev_b64 v[198:199], 11, v[200:201]
	v_lshlrev_b64 v[118:119], 11, v[118:119]
	v_lshl_add_u64 v[36:37], v[30:31], 0, v[36:37]
	v_lshl_add_u64 v[120:121], v[30:31], 0, v[120:121]
	v_lshl_add_u64 v[90:91], v[30:31], 0, v[90:91]
	v_lshl_add_u64 v[170:171], v[30:31], 0, v[170:171]
	v_lshl_add_u64 v[92:93], v[30:31], 0, v[92:93]
	v_lshl_add_u64 v[172:173], v[30:31], 0, v[172:173]
	v_lshl_add_u64 v[94:95], v[30:31], 0, v[94:95]
	v_lshl_add_u64 v[174:175], v[30:31], 0, v[174:175]
	v_lshl_add_u64 v[96:97], v[30:31], 0, v[96:97]
	v_lshl_add_u64 v[176:177], v[30:31], 0, v[176:177]
	v_lshl_add_u64 v[98:99], v[30:31], 0, v[98:99]
	v_lshl_add_u64 v[178:179], v[30:31], 0, v[178:179]
	v_lshl_add_u64 v[100:101], v[30:31], 0, v[100:101]
	v_lshl_add_u64 v[180:181], v[30:31], 0, v[180:181]
	v_lshl_add_u64 v[102:103], v[30:31], 0, v[102:103]
	v_lshl_add_u64 v[182:183], v[30:31], 0, v[182:183]
	v_lshl_add_u64 v[104:105], v[30:31], 0, v[104:105]
	v_lshl_add_u64 v[184:185], v[30:31], 0, v[184:185]
	v_lshl_add_u64 v[106:107], v[30:31], 0, v[106:107]
	v_lshl_add_u64 v[186:187], v[30:31], 0, v[186:187]
	v_lshl_add_u64 v[108:109], v[30:31], 0, v[108:109]
	v_lshl_add_u64 v[188:189], v[30:31], 0, v[188:189]
	v_lshl_add_u64 v[110:111], v[30:31], 0, v[110:111]
	v_lshl_add_u64 v[190:191], v[30:31], 0, v[190:191]
	v_lshl_add_u64 v[112:113], v[30:31], 0, v[112:113]
	v_lshl_add_u64 v[192:193], v[30:31], 0, v[192:193]
	v_lshl_add_u64 v[114:115], v[30:31], 0, v[114:115]
	v_lshl_add_u64 v[194:195], v[30:31], 0, v[194:195]
	v_lshl_add_u64 v[116:117], v[30:31], 0, v[116:117]
	v_lshl_add_u64 v[196:197], v[30:31], 0, v[196:197]
	v_lshl_add_u64 v[118:119], v[30:31], 0, v[118:119]
	v_lshl_add_u64 v[198:199], v[30:31], 0, v[198:199]
	s_waitcnt vmcnt(15)
	global_store_dwordx4 v[36:37], v[12:15], off sc1
	s_waitcnt vmcnt(15)
	global_store_dwordx4 v[36:37], v[16:19], off offset:1024 sc1
	global_store_dwordx4 v[120:121], v[12:15], off sc1
	global_store_dwordx4 v[120:121], v[16:19], off offset:1024 sc1
	global_store_dwordx4 v[90:91], v[12:15], off sc1
	global_store_dwordx4 v[90:91], v[16:19], off offset:1024 sc1
	global_store_dwordx4 v[170:171], v[12:15], off sc1
	global_store_dwordx4 v[170:171], v[16:19], off offset:1024 sc1
	s_waitcnt vmcnt(21)
	global_store_dwordx4 v[92:93], v[4:7], off sc1
	s_waitcnt vmcnt(21)
	global_store_dwordx4 v[92:93], v[8:11], off offset:1024 sc1
	global_store_dwordx4 v[172:173], v[4:7], off sc1
	global_store_dwordx4 v[172:173], v[8:11], off offset:1024 sc1
	global_store_dwordx4 v[94:95], v[4:7], off sc1
	global_store_dwordx4 v[94:95], v[8:11], off offset:1024 sc1
	global_store_dwordx4 v[174:175], v[4:7], off sc1
	global_store_dwordx4 v[174:175], v[8:11], off offset:1024 sc1
	s_waitcnt vmcnt(27)
	global_store_dwordx4 v[96:97], v[122:125], off sc1
	s_waitcnt vmcnt(27)
	global_store_dwordx4 v[96:97], v[126:129], off offset:1024 sc1
	global_store_dwordx4 v[176:177], v[122:125], off sc1
	global_store_dwordx4 v[176:177], v[126:129], off offset:1024 sc1
	global_store_dwordx4 v[98:99], v[122:125], off sc1
	global_store_dwordx4 v[98:99], v[126:129], off offset:1024 sc1
	global_store_dwordx4 v[178:179], v[122:125], off sc1
	global_store_dwordx4 v[178:179], v[126:129], off offset:1024 sc1
	s_waitcnt vmcnt(33)
	global_store_dwordx4 v[100:101], v[130:133], off sc1
	s_waitcnt vmcnt(33)
	global_store_dwordx4 v[100:101], v[134:137], off offset:1024 sc1
	global_store_dwordx4 v[180:181], v[130:133], off sc1
	global_store_dwordx4 v[180:181], v[134:137], off offset:1024 sc1
	global_store_dwordx4 v[102:103], v[130:133], off sc1
	global_store_dwordx4 v[102:103], v[134:137], off offset:1024 sc1
	global_store_dwordx4 v[182:183], v[130:133], off sc1
	global_store_dwordx4 v[182:183], v[134:137], off offset:1024 sc1
	s_waitcnt vmcnt(39)
	global_store_dwordx4 v[104:105], v[138:141], off sc1
	s_waitcnt vmcnt(39)
	global_store_dwordx4 v[104:105], v[142:145], off offset:1024 sc1
	global_store_dwordx4 v[184:185], v[138:141], off sc1
	global_store_dwordx4 v[184:185], v[142:145], off offset:1024 sc1
	global_store_dwordx4 v[106:107], v[138:141], off sc1
	global_store_dwordx4 v[106:107], v[142:145], off offset:1024 sc1
	global_store_dwordx4 v[186:187], v[138:141], off sc1
	global_store_dwordx4 v[186:187], v[142:145], off offset:1024 sc1
	s_waitcnt vmcnt(45)
	global_store_dwordx4 v[108:109], v[146:149], off sc1
	s_waitcnt vmcnt(45)
	global_store_dwordx4 v[108:109], v[150:153], off offset:1024 sc1
	global_store_dwordx4 v[188:189], v[146:149], off sc1
	global_store_dwordx4 v[188:189], v[150:153], off offset:1024 sc1
	global_store_dwordx4 v[110:111], v[146:149], off sc1
	global_store_dwordx4 v[110:111], v[150:153], off offset:1024 sc1
	global_store_dwordx4 v[190:191], v[146:149], off sc1
	global_store_dwordx4 v[190:191], v[150:153], off offset:1024 sc1
	s_waitcnt vmcnt(51)
	global_store_dwordx4 v[112:113], v[154:157], off sc1
	s_waitcnt vmcnt(51)
	global_store_dwordx4 v[112:113], v[158:161], off offset:1024 sc1
	global_store_dwordx4 v[192:193], v[154:157], off sc1
	global_store_dwordx4 v[192:193], v[158:161], off offset:1024 sc1
	global_store_dwordx4 v[114:115], v[154:157], off sc1
	global_store_dwordx4 v[114:115], v[158:161], off offset:1024 sc1
	global_store_dwordx4 v[194:195], v[154:157], off sc1
	global_store_dwordx4 v[194:195], v[158:161], off offset:1024 sc1
	s_waitcnt vmcnt(57)
	global_store_dwordx4 v[116:117], v[162:165], off sc1
	s_waitcnt vmcnt(57)
	global_store_dwordx4 v[116:117], v[166:169], off offset:1024 sc1
	global_store_dwordx4 v[196:197], v[162:165], off sc1
	global_store_dwordx4 v[196:197], v[166:169], off offset:1024 sc1
	global_store_dwordx4 v[118:119], v[162:165], off sc1
	global_store_dwordx4 v[118:119], v[166:169], off offset:1024 sc1
	global_store_dwordx4 v[198:199], v[162:165], off sc1
	global_store_dwordx4 v[198:199], v[166:169], off offset:1024 sc1
	s_cbranch_vccz .LBB0_2244

.LBB0_2256:
	s_mov_b32 s13, s12
	s_mov_b32 s14, s12
	s_mov_b32 s15, s12
	s_add_i32 s10, s10, 8
	v_mov_b64_e32 v[6:7], s[12:13]
	v_mov_b64_e32 v[8:9], s[14:15]
	v_cmp_lt_i32_e32 vcc, s10, v3
	global_store_dwordx4 v[4:5], v[6:9], off sc1
	global_store_dwordx4 v[4:5], v[6:9], off offset:1024 sc1
	v_lshl_add_u64 v[4:5], v[4:5], 0, s[42:43]
	s_cbranch_vccnz .LBB0_2256
	s_branch .LBB0_2220
